# prologue: the S5 discretisation block of workgroup 248 (which now carries a third hyena task) moves to workgroup 247
# baseline (speedup 1.0000x reference)
; __device__ __forceinline__ bfr f2bf(float f) { return (bfr)(pack2(f, 0.f) & 0xffffu); }
;     ...
;     for (int i = bid * NTHR + tid; i < 4096; i += nb * NTHR) {
;         const int dg = i >> 6, p = i & 63;
;         const float are = P.in[26][i], aim = P.in[27][i];
;         const float dt = expf(P.in[28][dg]);
;         const float mag = expf(are * dt);
;         const float abr = mag * cosf(aim * dt), abi = mag * sinf(aim * dt);
;         ((float2*)(P.ws + WS_ABAR))[i] = make_float2(abr, abi);
;         float xr = abr, xi = abi;
; #pragma unroll
;         for (int q = 0; q < 6; ++q) { const float nr = xr * xr - xi * xi, ni = 2.f * xr * xi; xr = nr; xi = ni; }
;         ((float2*)(P.ws + WS_A64))[i] = make_float2(xr, xi);
;         const float nr = abr - 1.f, ni = abi, den = are * are + aim * aim;
;         const float cr = (nr * are + ni * aim) / den, ci = (ni * are - nr * aim) / den;
;         float2* bb = (float2*)(P.ws + WS_BBAR) + (size_t)i * 16;
; #pragma unroll 4
;         for (int k = 0; k < 16; ++k) {
;             const float br = P.in[29][(size_t)i * 16 + k], bi = P.in[30][(size_t)i * 16 + k];
;             bb[k] = make_float2(cr * br - ci * bi, cr * bi + ci * br);
;         }
;         bfr* cm = (bfr*)(P.ws + WS_CMAT) + (size_t)dg * 16 * 128;
; #pragma unroll 4
;         for (int n = 0; n < 16; ++n) {
;             const float c_re = P.in[31][((size_t)dg * 16 + n) * 64 + p], c_im = P.in[32][((size_t)dg * 16 + n) * 64 + p];
;             cm[n * 128 + 2 * p] = f2bf(c_re); cm[n * 128 + 2 * p + 1] = f2bf(-c_im);
;         }
;     }
.LBB0_280:
	s_xor_b32 s0, s44, 0xff
	s_cmp_eq_u32 s0, 8
	s_cselect_b32 s96, 7, s0
	s_cmp_eq_u32 s0, 7
	s_cselect_b32 s0, 8, s96
	v_lshl_or_b32 v2, s0, 9, v0
	s_movk_i32 s0, 0x1000
	v_cmp_gt_i32_e32 vcc, s0, v2
	s_and_saveexec_b64 s[2:3], vcc
	s_cbranch_execz .LBB0_295
	v_readlane_b32 s16, v252, 19
	s_lshl_b32 s4, s4, 9
	v_readlane_b32 s18, v252, 21
	v_readlane_b32 s19, v252, 22
	s_add_u32 s10, s18, 0x4f28000
	s_addc_u32 s11, s19, 0
	s_add_u32 s12, s18, 0x4f30000
	s_addc_u32 s13, s19, 0
	v_ashrrev_i32_e32 v3, 31, v2
	s_add_u32 s14, s18, 0x4fb8000
	v_lshlrev_b64 v[6:7], 7, v[2:3]
	v_lshlrev_b32_e32 v4, 1, v202
	v_readlane_b32 s17, v252, 20
	s_addc_u32 s15, s19, 0
	v_lshl_add_u64 v[6:7], s[18:19], 0, v[6:7]
	s_mov_b64 s[0:1], 0x4f38018
	s_ashr_i32 s5, s4, 31
	v_lshlrev_b64 v[10:11], 6, v[2:3]
	v_mov_b32_e32 v1, v4
	v_lshl_add_u64 v[6:7], v[6:7], 0, s[0:1]
	s_lshl_b64 s[16:17], s[4:5], 7
	v_lshl_add_u64 v[8:9], s[64:65], 0, v[10:11]
	s_lshl_b64 s[18:19], s[4:5], 6
	v_lshl_add_u64 v[10:11], s[62:63], 0, v[10:11]
	s_mov_b64 s[20:21], 0
	s_mov_b32 s5, 0x3fb8aa3b
	s_mov_b32 s28, 0xc2ce8ed0
	s_mov_b32 s23, 0
	s_mov_b32 s29, 0x42b17218
	v_mov_b32_e32 v5, 0x7f800000
	s_mov_b32 s30, 0xfe5163ab
	v_mov_b32_e32 v13, 0
	s_mov_b32 s31, 0x3c439041
	s_mov_b32 s34, 0xdb629599
	s_mov_b32 s35, 0xf534ddc0
	s_mov_b32 s36, 0xfc2757d1
	s_mov_b32 s37, 0x4e441529
	s_mov_b32 s38, 0xa2f9836e
	s_mov_b32 s39, 0x3fc90fda
	s_mov_b32 s40, 0xbfc90fda
	v_mov_b32_e32 v24, 0x3c0881c4
	v_mov_b32_e32 v25, 0xbab64f3b
	v_mov_b32_e32 v15, 2.0
	v_not_b32_e32 v26, 63
	v_not_b32_e32 v27, 31
	v_mov_b32_e32 v28, 0x7fc00000
